# lever 6 (LDS bank conflicts): XOR-swizzled chunk index for the f32 N diagonal-block image (8-way conflicted ds_write_b128 in T3a stage E; reader = stage F substitution)
# speedup vs baseline: 1.0013x; 1.0013x over previous
; __device__ __forceinline__ int crow(int reg, int h) { return (reg & 3) + 8 * (reg >> 2) + 4 * h; }
; __device__ __forceinline__ f32x16 zero16() { return (f32x16){0.f, 0.f, 0.f, 0.f, 0.f, 0.f, 0.f, 0.f, 0.f, 0.f, 0.f, 0.f, 0.f, 0.f, 0.f, 0.f}; }
; __device__ __forceinline__ void phase1(const int WID_, const In& I, char* lds) {
;     ...
;             const int mat = tid >> 7, row = (tid >> 2) & 31, chunk = tid & 3;
;             *(uint4*)(MAT(O_NM + mat * MB) + row * LD + 32 + chunk * 8) = make_uint4(0, 0, 0, 0);
;         }
;         for (int task = wv; task < 12; task += 8) {
;             const int mat = task / 3, tt = task % 3, st = (tt == 0) ? 0 : 1, jt = (tt == 2) ? 1 : 0;
;             const bf16* Asrc = MAT((mat & 1) ? O_KB : O_BB) + 32 * jt * LD;
;             const bf16* Bsrc = MAT((mat >> 1) ? O_RB : O_AB) + 32 * st * LD;
;             f32x16 acc = mm_tile<64>(zero16(), Asrc, LD, Bsrc, LD, lane);
;             const int cs = 32 * st + (lane & 31), hh = lane >> 5; const bool incl = (mat >> 1) != 0;
; #pragma unroll
;             for (int rg = 0; rg < 16; ++rg) { const int j = 32 * jt + crow(rg, hh); const bool keep = incl ? (j <= cs) : (j < cs); if (!keep) acc[rg] = 0.f; }
;             store_tr(acc, MAT(O_NM + mat * MB) + 32 * st * LD + 32 * jt, LD, lane);
;             if (mat == 0 && st == jt) {
;                 float* d = NMF + st * 1024 + (lane & 31) * 32;
.LBB0_1428:
	s_or_b64 exec, exec, s[0:1]
	v_lshrrev_b32_e32 v0, 7, v59
	v_bfe_u32 v1, v59, 2, 5
	s_movk_i32 s0, 0x2400
	v_mul_lo_u32 v0, v0, s0
	v_mul_u32_u24_e32 v1, 0x90, v1
	v_add3_u32 v0, 0, v0, v1
	v_lshlrev_b32_e32 v1, 4, v58
	v_and_b32_e32 v1, 48, v1
	s_mov_b32 s0, 0x14440
	v_and_b32_e32 v78, 31, v58
	v_ashrrev_i32_e32 v57, 2, v58
	v_ashrrev_i32_e32 v79, 5, v58
	v_ashrrev_i32_e32 v56, 3, v58
	v_add3_u32 v0, v0, v1, s0
	s_andn2_b64 vcc, exec, s[2:3]
	v_mul_u32_u24_e32 v53, 0x48, v78
	v_and_b32_e32 v54, -8, v57
	v_lshlrev_b32_e32 v52, 2, v79
	v_and_b32_e32 v55, -4, v56
	ds_write_b128 v0, v[16:19]
	s_cbranch_vccnz .LBB0_1438
	v_and_b32_e32 v0, -8, v57
	v_and_b32_e32 v1, -4, v56
	v_lshlrev_b32_e32 v2, 7, v78
	v_and_b32_e32 v3, 1, v78
	v_xor_b32_e32 v3, v79, v3
	v_lshlrev_b32_e32 v3, 4, v3
	v_lshlrev_b32_e32 v89, 4, v78
	v_and_b32_e32 v89, 0x60, v89
	v_add3_u32 v59, s77, v2, v3
	v_lshlrev_b32_e32 v60, 1, v53
	v_lshlrev_b32_e32 v61, 1, v0
	v_lshlrev_b32_e32 v62, 1, v1
	v_readlane_b32 s4, v243, 44
	s_branch .LBB0_1431

; __device__ __forceinline__ void phase1(const int WID_, const In& I, char* lds) {
;     ...
;             if (mat == 0 && st == jt) {
;                 float* d = NMF + st * 1024 + (lane & 31) * 32;
; #pragma unroll
;                 for (int g = 0; g < 4; ++g) *(float4*)(d + 8 * g + 4 * hh) = make_float4(acc[4 * g], acc[4 * g + 1], acc[4 * g + 2], acc[4 * g + 3]);
;             }
.LBB0_1436:
	s_andn2_b64 vcc, exec, s[0:1]
	s_cbranch_vccnz .LBB0_1430
	s_and_b64 s[0:1], s[6:7], exec
	s_cselect_b32 s0, 0, 0x1000
	v_add_u32_e32 v63, s0, v59
	v_add_u32_e32 v64, v63, v89
	v_xor_b32_e32 v65, 32, v89
	v_xor_b32_e32 v66, 64, v89
	v_xor_b32_e32 v67, 0x60, v89
	v_add_u32_e32 v65, v63, v65
	v_add_u32_e32 v66, v63, v66
	v_add_u32_e32 v67, v63, v67
	ds_write_b128 v64, v[0:3]
	ds_write_b128 v65, v[4:7]
	ds_write_b128 v66, v[8:11]
	ds_write_b128 v67, v[12:15]
	s_branch .LBB0_1430

; __device__ __forceinline__ void phase1(const int WID_, const In& I, char* lds) {
;     ...
;         if (wv == 0) {
;             const int d = lane >> 4, cc = lane & 15;
;             const float* nb = NMF + (d >> 1) * 1024 + (16 * (d & 1)) * 32 + 16 * (d & 1);
;             float T[16];
; #pragma unroll
;             for (int i = 0; i < 16; ++i) {
;                 float acc = (i == cc) ? 1.f : 0.f;
; #pragma unroll
;                 for (int j4 = 0; j4 < i; j4 += 4) { const float4 n4 = *(const float4*)(nb + i * 32 + j4);
;                     acc += n4.x * T[j4]; if (j4 + 1 < i) acc += n4.y * T[j4 + 1]; if (j4 + 2 < i) acc += n4.z * T[j4 + 2]; if (j4 + 3 < i) acc += n4.w * T[j4 + 3]; }
;                 T[i] = acc;
;             }
.LBB0_1446:
	v_and_b32_e32 v80, 15, v58
	s_andn2_b64 vcc, exec, s[0:1]
	v_lshlrev_b32_e32 v10, 1, v80
	v_mul_u32_u24_e32 v59, 0x50, v78
	s_cbranch_vccnz .LBB0_1448
	v_lshlrev_b32_e32 v60, 7, v58
	v_and_b32_e32 v60, 0xfffff000, v60
	v_and_b32_e32 v61, 16, v58
	v_add_u32_e32 v60, s77, v60
	v_lshlrev_b32_e32 v74, 7, v61
	v_lshlrev_b32_e32 v75, 2, v61
	v_add3_u32 v81, v60, v74, v75
	v_xor_b32_e32 v75, 64, v81
	ds_read_b128 v[86:89], v81 offset:144
	ds_read_b128 v[90:93], v81 offset:288
	ds_read_b128 v[94:97], v81 offset:432
	ds_read_b128 v[98:101], v75 offset:512
	ds_read_b128 v[102:105], v75 offset:656
	ds_read_b128 v[106:109], v75 offset:800
	ds_read_b128 v[110:113], v75 offset:944
	ds_read_b128 v[114:117], v81 offset:1024
	ds_read_b128 v[118:121], v81 offset:1168
	ds_read_b128 v[122:125], v81 offset:1312
	ds_read_b128 v[126:129], v81 offset:1456
	ds_read_b128 v[130:133], v75 offset:1536
	ds_read_b128 v[134:137], v75 offset:1680
	ds_read_b128 v[138:141], v75 offset:1824
	ds_read_b128 v[142:145], v75 offset:1968
	v_cmp_eq_u32_e32 vcc, 0, v80
	v_cmp_eq_u32_e64 s[98:99], 1, v80
	v_cmp_eq_u32_e64 s[100:101], 2, v80
	v_cndmask_b32_e64 v0, 0, 1.0, vcc
	v_cmp_eq_u32_e32 vcc, 3, v80
	v_cndmask_b32_e64 v1, 0, 1.0, s[98:99]
	v_cmp_eq_u32_e64 s[98:99], 4, v80
	v_cndmask_b32_e64 v2, 0, 1.0, s[100:101]
	v_cmp_eq_u32_e64 s[100:101], 5, v80
	v_cndmask_b32_e64 v3, 0, 1.0, vcc
	v_cmp_eq_u32_e32 vcc, 6, v80
	v_cndmask_b32_e64 v4, 0, 1.0, s[98:99]
	v_cmp_eq_u32_e64 s[98:99], 7, v80
	v_cndmask_b32_e64 v5, 0, 1.0, s[100:101]
	v_cmp_eq_u32_e64 s[100:101], 8, v80
	v_cndmask_b32_e64 v6, 0, 1.0, vcc
	v_cmp_eq_u32_e32 vcc, 9, v80
	v_cndmask_b32_e64 v7, 0, 1.0, s[98:99]
	v_cmp_eq_u32_e64 s[98:99], 10, v80
	v_cndmask_b32_e64 v8, 0, 1.0, s[100:101]
	v_cmp_eq_u32_e64 s[100:101], 11, v80
	v_cndmask_b32_e64 v9, 0, 1.0, vcc
	v_cmp_eq_u32_e32 vcc, 12, v80
	v_cndmask_b32_e64 v11, 0, 1.0, s[98:99]
	v_cmp_eq_u32_e64 s[98:99], 13, v80
	v_cndmask_b32_e64 v12, 0, 1.0, s[100:101]
	v_cmp_eq_u32_e64 s[100:101], 14, v80
	v_cndmask_b32_e64 v13, 0, 1.0, vcc
	v_cmp_eq_u32_e32 vcc, 15, v80
	v_cndmask_b32_e64 v14, 0, 1.0, s[98:99]
	v_cndmask_b32_e64 v15, 0, 1.0, s[100:101]
	v_cndmask_b32_e64 v68, 0, 1.0, vcc
	s_waitcnt lgkmcnt(14)
	v_fmac_f32_e32 v1, v86, v0
	s_waitcnt lgkmcnt(13)
	v_fmac_f32_e32 v2, v90, v0
	s_waitcnt lgkmcnt(12)
	v_fmac_f32_e32 v3, v94, v0
	s_waitcnt lgkmcnt(11)
	v_fmac_f32_e32 v4, v98, v0
	s_waitcnt lgkmcnt(10)
	v_fmac_f32_e32 v5, v102, v0
	s_waitcnt lgkmcnt(9)
	v_fmac_f32_e32 v6, v106, v0
	s_waitcnt lgkmcnt(8)
	v_fmac_f32_e32 v7, v110, v0
	s_waitcnt lgkmcnt(7)
	v_fmac_f32_e32 v8, v114, v0
	s_waitcnt lgkmcnt(6)
	v_fmac_f32_e32 v9, v118, v0
	s_waitcnt lgkmcnt(5)
	v_fmac_f32_e32 v11, v122, v0
	s_waitcnt lgkmcnt(4)
	v_fmac_f32_e32 v12, v126, v0
	s_waitcnt lgkmcnt(3)
	v_fmac_f32_e32 v13, v130, v0
	s_waitcnt lgkmcnt(2)
	v_fmac_f32_e32 v14, v134, v0
	s_waitcnt lgkmcnt(1)
	v_fmac_f32_e32 v15, v138, v0
	s_waitcnt lgkmcnt(0)
	v_fmac_f32_e32 v68, v142, v0
	ds_read_b128 v[146:149], v75 offset:640
	ds_read_b128 v[150:153], v75 offset:816
	ds_read_b128 v[154:157], v75 offset:928
	ds_read_b128 v[158:161], v81 offset:1040
	ds_read_b128 v[162:165], v81 offset:1152
	ds_read_b128 v[166:169], v81 offset:1328
	ds_read_b128 v[170:173], v81 offset:1440
	ds_read_b128 v[60:63], v75 offset:1552
	ds_read_b128 v[64:67], v75 offset:1664
	ds_read_b128 v[70:73], v75 offset:1840
	ds_read_b128 v[82:85], v75 offset:1952
	v_fmac_f32_e32 v2, v91, v1
	v_fmac_f32_e32 v3, v95, v1
	v_fmac_f32_e32 v4, v99, v1
	v_fmac_f32_e32 v5, v103, v1
	v_fmac_f32_e32 v6, v107, v1
	v_fmac_f32_e32 v7, v111, v1
	v_fmac_f32_e32 v8, v115, v1
	v_fmac_f32_e32 v9, v119, v1
	v_fmac_f32_e32 v11, v123, v1
	v_fmac_f32_e32 v12, v127, v1
	v_fmac_f32_e32 v13, v131, v1
	v_fmac_f32_e32 v14, v135, v1
	v_fmac_f32_e32 v15, v139, v1
	v_fmac_f32_e32 v68, v143, v1
	v_fmac_f32_e32 v3, v96, v2
	v_fmac_f32_e32 v4, v100, v2
	v_fmac_f32_e32 v5, v104, v2
	v_fmac_f32_e32 v6, v108, v2
	v_fmac_f32_e32 v7, v112, v2
	v_fmac_f32_e32 v8, v116, v2
	v_fmac_f32_e32 v9, v120, v2
	v_fmac_f32_e32 v11, v124, v2
	v_fmac_f32_e32 v12, v128, v2
	v_fmac_f32_e32 v13, v132, v2
	v_fmac_f32_e32 v14, v136, v2
	v_fmac_f32_e32 v15, v140, v2
	v_fmac_f32_e32 v68, v144, v2
	v_fmac_f32_e32 v4, v101, v3
	v_fmac_f32_e32 v5, v105, v3
	v_fmac_f32_e32 v6, v109, v3
	v_fmac_f32_e32 v7, v113, v3
	v_fmac_f32_e32 v8, v117, v3
	v_fmac_f32_e32 v9, v121, v3
	v_fmac_f32_e32 v11, v125, v3
	v_fmac_f32_e32 v12, v129, v3
	v_fmac_f32_e32 v13, v133, v3
	v_fmac_f32_e32 v14, v137, v3
	v_fmac_f32_e32 v15, v141, v3
	v_fmac_f32_e32 v68, v145, v3
	s_waitcnt lgkmcnt(0)
; __device__ __forceinline__ unsigned pk2(float lo, float hi) { const f32x2h v = {lo, hi}; const bf16x2h b = __builtin_convertvector(v, bf16x2h); return __builtin_bit_cast(unsigned, b); }
; __device__ __forceinline__ bf16 f2bf(float f) { return (bf16)(pk2(f, f) & 0xffffu); }
; __device__ __forceinline__ void phase1(const int WID_, const In& I, char* lds) {
;     ...
;             for (int i = 0; i < 16; ++i) {
;                 float acc = (i == cc) ? 1.f : 0.f;
; #pragma unroll
;                 for (int j4 = 0; j4 < i; j4 += 4) { const float4 n4 = *(const float4*)(nb + i * 32 + j4);
;                     acc += n4.x * T[j4]; if (j4 + 1 < i) acc += n4.y * T[j4 + 1]; if (j4 + 2 < i) acc += n4.z * T[j4 + 2]; if (j4 + 3 < i) acc += n4.w * T[j4 + 3]; }
;                 T[i] = acc;
;             }
;             bf16* tm = MAT(O_TM) + (16 * d) * LD + 16 * d + cc;
; #pragma unroll
;             for (int i = 0; i < 16; ++i) tm[i * LD] = f2bf(T[i]);
;             bf16* tt = MAT(O_TT) + (d >> 1) * 32 * 40 + (16 * (d & 1) + cc) * 40 + 16 * (d & 1);
;             *(uint4*)(tt) = make_uint4(pk2(T[0], T[1]), pk2(T[2], T[3]), pk2(T[4], T[5]), pk2(T[6], T[7]));
;             *(uint4*)(tt + 8) = make_uint4(pk2(T[8], T[9]), pk2(T[10], T[11]), pk2(T[12], T[13]), pk2(T[14], T[15]));
;             { const int blk = lane >> 5, r16 = (lane >> 1) & 15, hf = lane & 1;
;               *(uint4*)(MAT(O_TM) + (32 * blk + r16) * LD + 32 * blk + 16 + 8 * hf) = make_uint4(0, 0, 0, 0);
;               *(uint4*)(MAT(O_TT) + blk * 32 * 40 + (16 + r16) * 40 + 8 * hf) = make_uint4(0, 0, 0, 0); }
	ds_read_b128 v[86:89], v81 offset:1200
	ds_read_b128 v[90:93], v81 offset:1280
	ds_read_b128 v[94:97], v81 offset:1424
	ds_read_b128 v[98:101], v75 offset:1568
	ds_read_b128 v[102:105], v75 offset:1712
	ds_read_b128 v[106:109], v75 offset:1792
	ds_read_b128 v[110:113], v75 offset:1936
	ds_read_b128 v[114:117], v75 offset:1696
	ds_read_b128 v[118:121], v75 offset:1808
	ds_read_b128 v[122:125], v75 offset:1920
	v_fmac_f32_e32 v5, v146, v4
	v_fmac_f32_e32 v6, v150, v4
	v_fmac_f32_e32 v7, v154, v4
	v_fmac_f32_e32 v8, v158, v4
	v_fmac_f32_e32 v9, v162, v4
	v_fmac_f32_e32 v11, v166, v4
	v_fmac_f32_e32 v12, v170, v4
	v_fmac_f32_e32 v13, v60, v4
	v_fmac_f32_e32 v14, v64, v4
	v_fmac_f32_e32 v15, v70, v4
	v_fmac_f32_e32 v68, v82, v4
	v_fmac_f32_e32 v6, v151, v5
	v_fmac_f32_e32 v7, v155, v5
	v_fmac_f32_e32 v8, v159, v5
	v_fmac_f32_e32 v9, v163, v5
	v_fmac_f32_e32 v11, v167, v5
	v_fmac_f32_e32 v12, v171, v5
	v_fmac_f32_e32 v13, v61, v5
	v_fmac_f32_e32 v14, v65, v5
	v_fmac_f32_e32 v15, v71, v5
	v_fmac_f32_e32 v68, v83, v5
	v_fmac_f32_e32 v7, v156, v6
	v_fmac_f32_e32 v8, v160, v6
	v_fmac_f32_e32 v9, v164, v6
	v_fmac_f32_e32 v11, v168, v6
	v_fmac_f32_e32 v12, v172, v6
	v_fmac_f32_e32 v13, v62, v6
	v_fmac_f32_e32 v14, v66, v6
	v_fmac_f32_e32 v15, v72, v6
	v_fmac_f32_e32 v68, v84, v6
	v_fmac_f32_e32 v8, v161, v7
	v_fmac_f32_e32 v9, v165, v7
	v_fmac_f32_e32 v11, v169, v7
	v_fmac_f32_e32 v12, v173, v7
	v_fmac_f32_e32 v13, v63, v7
	v_fmac_f32_e32 v14, v67, v7
	v_fmac_f32_e32 v15, v73, v7
	v_fmac_f32_e32 v68, v85, v7
	s_waitcnt lgkmcnt(0)
	v_fmac_f32_e32 v9, v86, v8
	v_fmac_f32_e32 v11, v90, v8
	v_fmac_f32_e32 v12, v94, v8
	v_fmac_f32_e32 v13, v98, v8
	v_fmac_f32_e32 v14, v102, v8
	v_fmac_f32_e32 v15, v106, v8
	v_fmac_f32_e32 v68, v110, v8
	v_fmac_f32_e32 v11, v91, v9
	v_fmac_f32_e32 v12, v95, v9
	v_fmac_f32_e32 v13, v99, v9
	v_fmac_f32_e32 v14, v103, v9
	v_fmac_f32_e32 v15, v107, v9
	v_fmac_f32_e32 v68, v111, v9
	v_fmac_f32_e32 v12, v96, v11
	v_fmac_f32_e32 v13, v100, v11
	v_fmac_f32_e32 v14, v104, v11
	v_fmac_f32_e32 v15, v108, v11
	v_fmac_f32_e32 v68, v112, v11
	v_fmac_f32_e32 v13, v101, v12
	v_fmac_f32_e32 v14, v105, v12
	v_fmac_f32_e32 v15, v109, v12
	v_fmac_f32_e32 v68, v113, v12
	v_fmac_f32_e32 v14, v114, v13
	v_fmac_f32_e32 v15, v118, v13
	v_fmac_f32_e32 v68, v122, v13
	v_fmac_f32_e32 v15, v119, v14
	v_fmac_f32_e32 v68, v123, v14
	v_fmac_f32_e32 v68, v124, v15
	v_cvt_pk_bf16_f32 v146, v0, v1
	v_cvt_pk_bf16_f32 v147, v2, v3
	v_cvt_pk_bf16_f32 v148, v4, v5
	v_cvt_pk_bf16_f32 v149, v6, v7
	v_cvt_pk_bf16_f32 v150, v8, v9
	v_cvt_pk_bf16_f32 v151, v11, v12
	v_cvt_pk_bf16_f32 v152, v13, v14
	v_cvt_pk_bf16_f32 v153, v15, v68
	v_and_b32_e32 v60, -16, v58
	v_mul_lo_u32 v74, v60, s9
	v_lshlrev_b32_e32 v60, 1, v60
	v_add3_u32 v74, v74, v60, v10
	ds_write_b16 v74, v146
	ds_write_b16_d16_hi v74, v146 offset:144
	ds_write_b16 v74, v147 offset:288
	ds_write_b16_d16_hi v74, v147 offset:432
	ds_write_b16 v74, v148 offset:576
	ds_write_b16_d16_hi v74, v148 offset:720
	ds_write_b16 v74, v149 offset:864
	ds_write_b16_d16_hi v74, v149 offset:1008
	ds_write_b16 v74, v150 offset:1152
	ds_write_b16_d16_hi v74, v150 offset:1296
	ds_write_b16 v74, v151 offset:1440
	ds_write_b16_d16_hi v74, v151 offset:1584
	ds_write_b16 v74, v152 offset:1728
	ds_write_b16_d16_hi v74, v152 offset:1872
	ds_write_b16 v74, v153 offset:2016
	ds_write_b16_d16_hi v74, v153 offset:2160
	v_and_b32_e32 v8, 0xffffffe0, v58
	s_movk_i32 s0, 0x50
	v_mul_lo_u32 v60, v8, s0
	s_add_i32 s0, 0, 0x1f400
	v_add_u32_e32 v11, s0, v60
	v_and_b32_e32 v61, 16, v58
	v_lshlrev_b32_e32 v61, 1, v61
	v_add3_u32 v75, v11, v59, v61
	ds_write_b128 v75, v[146:149]
	ds_write_b128 v75, v[150:153] offset:16
	v_bfe_u32 v0, v58, 1, 4
	v_lshlrev_b32_e32 v6, 3, v58
	v_or_b32_e32 v1, v0, v8
	v_mul_lo_u32 v1, v1, s9
	v_lshlrev_b32_e32 v3, 1, v6
	s_mov_b32 s4, s5
	v_add_u32_e32 v1, 0, v1
	v_lshlrev_b32_e32 v2, 1, v8
	v_and_b32_e32 v3, 16, v3
	s_mov_b32 s6, s5
	s_mov_b32 s7, s5
	v_mov_b64_e32 v[4:5], s[4:5]
	v_mul_u32_u24_e32 v0, 0x50, v0
	v_add3_u32 v1, v1, v2, v3
	v_mov_b64_e32 v[6:7], s[6:7]
	v_add3_u32 v0, v11, v0, v3
	ds_write_b128 v1, v[4:7] offset:32
	ds_write_b128 v0, v[4:7] offset:1280
